# baseline (speedup 1.0000x reference)
.Lu0_1:
	ds_read_b64_tr_b16 v[178:179], v206 offset:24576
	ds_read_b64_tr_b16 v[180:181], v206 offset:25600
	s_waitcnt lgkmcnt(9)
	v_mfma_f32_32x32x16_f16 v[98:113], v[82:85], v[154:157], v[34:49]
	v_add_f32_e32 v224, v66, v70
	v_add_f32_e32 v225, v67, v71
	v_add_f32_e32 v226, v68, v72
	v_add_f32_e32 v227, v69, v73
	v_cvt_pk_f16_f32 v158, v66, v67
	v_cvt_pk_f16_f32 v159, v68, v69
	ds_read_b64_tr_b16 v[174:175], v207 offset:24576
	ds_read_b64_tr_b16 v[176:177], v207 offset:25600
	s_waitcnt lgkmcnt(10)
	v_mfma_f32_32x32x16_f16 v[82:97], v[170:173], v[154:157], v[34:49]
	v_add_f32_e32 v224, v74, v224
	v_add_f32_e32 v225, v75, v225
	v_add_f32_e32 v226, v76, v226
	v_add_f32_e32 v227, v77, v227
	v_cvt_pk_f16_f32 v160, v70, v71
	v_cvt_pk_f16_f32 v161, v72, v73
	ds_read_b64_tr_b16 v[170:171], v206 offset:26624
	ds_read_b64_tr_b16 v[172:173], v206 offset:27648
	s_waitcnt lgkmcnt(11)
	v_mfma_f32_32x32x16_f16 v[98:113], v[166:169], v[146:149], v[98:113]
	v_add_f32_e32 v224, v78, v224
	v_add_f32_e32 v225, v79, v225
	v_add_f32_e32 v226, v80, v226
	v_add_f32_e32 v227, v81, v227
	v_cvt_pk_f16_f32 v150, v74, v75
	v_cvt_pk_f16_f32 v151, v76, v77
	ds_read_b64_tr_b16 v[74:75], v207 offset:26624
	ds_read_b64_tr_b16 v[76:77], v207 offset:27648
	s_waitcnt lgkmcnt(12)
	v_mfma_f32_32x32x16_f16 v[82:97], v[162:165], v[146:149], v[82:97]
	v_add_f32_e32 v224, v50, v224
	v_add_f32_e32 v225, v51, v225
	v_add_f32_e32 v226, v52, v226
	v_add_f32_e32 v227, v53, v227
	v_cvt_pk_f16_f32 v152, v78, v79
	v_cvt_pk_f16_f32 v153, v80, v81
	ds_read_b64_tr_b16 v[70:71], v206 offset:28672
	ds_read_b64_tr_b16 v[72:73], v206 offset:29696
	s_waitcnt lgkmcnt(13)
	v_mfma_f32_32x32x16_f16 v[98:113], v[126:129], v[138:141], v[98:113]
	v_add_f32_e32 v224, v54, v224
	v_add_f32_e32 v225, v55, v225
	v_add_f32_e32 v226, v56, v226
	v_add_f32_e32 v227, v57, v227
	v_cvt_pk_f16_f32 v142, v50, v51
	v_cvt_pk_f16_f32 v143, v52, v53
	ds_read_b64_tr_b16 v[66:67], v207 offset:28672
	ds_read_b64_tr_b16 v[68:69], v207 offset:29696
	s_waitcnt lgkmcnt(14)
	v_mfma_f32_32x32x16_f16 v[82:97], v[122:125], v[138:141], v[82:97]
	v_add_f32_e32 v224, v58, v224
	v_add_f32_e32 v225, v59, v225
	v_add_f32_e32 v226, v60, v226
	v_add_f32_e32 v227, v61, v227
	v_cvt_pk_f16_f32 v144, v54, v55
	v_cvt_pk_f16_f32 v145, v56, v57
	ds_read_b64_tr_b16 v[54:55], v206 offset:30720
	ds_read_b64_tr_b16 v[56:57], v206 offset:31744
	s_waitcnt lgkmcnt(14)
	v_mfma_f32_32x32x16_f16 v[98:113], v[118:121], v[134:137], v[98:113]
	v_add_f32_e32 v224, v62, v224
	v_add_f32_e32 v225, v63, v225
	v_add_f32_e32 v226, v64, v226
	v_add_f32_e32 v227, v65, v227
	v_cvt_pk_f16_f32 v130, v58, v59
	v_cvt_pk_f16_f32 v131, v60, v61
	ds_read_b64_tr_b16 v[50:51], v207 offset:30720
	ds_read_b64_tr_b16 v[52:53], v207 offset:31744
	v_mfma_f32_32x32x16_f16 v[82:97], v[114:117], v[134:137], v[82:97]
	v_add_f32_e32 v224, v224, v225
	v_add_f32_e32 v226, v226, v227
	v_add_f32_e32 v60, v224, v226
	v_cvt_pk_f16_f32 v132, v62, v63
	v_cvt_pk_f16_f32 v133, v64, v65
	s_add_i32 s26, s42, s36
	s_mov_b32 m0, s26
	s_nop 0
	global_load_lds_dwordx4 v221, s[50:51]
	s_add_i32 s26, s39, s35
	s_mov_b32 m0, s26
	s_nop 0
	global_load_lds_dwordx4 v222, s[52:53]
	v_max3_f32 v58, v98, v99, v100
	v_max3_f32 v59, v101, v102, v103
	v_max3_f32 v228, v104, v105, v106
	v_max3_f32 v229, v107, v108, v109
	v_max3_f32 v58, v58, v110, v111
	v_max3_f32 v59, v59, v112, v113
	v_max3_f32 v228, v228, v82, v83
	v_max3_f32 v229, v229, v84, v85
	v_max3_f32 v58, v58, v86, v87
	v_max3_f32 v59, v59, v88, v89
	v_max3_f32 v228, v228, v90, v91
	v_max3_f32 v229, v229, v92, v93
	v_max3_f32 v58, v58, v94, v95
	v_max3_f32 v59, v59, v96, v97
	v_max3_f32 v58, v58, v59, v228
	v_max_f32_e32 v58, v58, v229
	v_add_f32_e32 v198, v183, v60
	v_cmp_lt_f32_e32 vcc, s41, v58
	s_cmp_lg_u64 vcc, 0
	s_cselect_b64 s[26:27], -1, 0
	s_cbranch_vccnz .Lu0_9

.Lu0_4:
	s_add_i32 s26, s39, 0x2000
	s_cmpk_lg_i32 s39, 0x4000
	s_cselect_b32 s43, s26, 0
	ds_read_b64_tr_b16 v[126:127], v206 offset:32768
	ds_read_b64_tr_b16 v[128:129], v206 offset:33792
	s_waitcnt lgkmcnt(9)
	v_mfma_f32_32x32x16_f16 v[66:81], v[58:61], v[154:157], v[34:49]
	v_add_f32_e32 v224, v98, v102
	v_add_f32_e32 v225, v99, v103
	v_add_f32_e32 v226, v100, v104
	v_add_f32_e32 v227, v101, v105
	v_cvt_pk_f16_f32 v158, v98, v99
	v_cvt_pk_f16_f32 v159, v100, v101
	ds_read_b64_tr_b16 v[122:123], v207 offset:32768
	ds_read_b64_tr_b16 v[124:125], v207 offset:33792
	s_waitcnt lgkmcnt(10)
	v_mfma_f32_32x32x16_f16 v[50:65], v[114:117], v[154:157], v[34:49]
	v_add_f32_e32 v224, v106, v224
	v_add_f32_e32 v225, v107, v225
	v_add_f32_e32 v226, v108, v226
	v_add_f32_e32 v227, v109, v227
	v_cvt_pk_f16_f32 v160, v102, v103
	v_cvt_pk_f16_f32 v161, v104, v105
	ds_read_b64_tr_b16 v[118:119], v206 offset:34816
	ds_read_b64_tr_b16 v[120:121], v206 offset:35840
	s_waitcnt lgkmcnt(11)
	v_mfma_f32_32x32x16_f16 v[66:81], v[182:185], v[146:149], v[66:81]
	v_add_f32_e32 v224, v110, v224
	v_add_f32_e32 v225, v111, v225
	v_add_f32_e32 v226, v112, v226
	v_add_f32_e32 v227, v113, v227
	v_cvt_pk_f16_f32 v150, v106, v107
	v_cvt_pk_f16_f32 v151, v108, v109
	ds_read_b64_tr_b16 v[114:115], v207 offset:34816
	ds_read_b64_tr_b16 v[116:117], v207 offset:35840
	s_waitcnt lgkmcnt(12)
	v_mfma_f32_32x32x16_f16 v[50:65], v[174:177], v[146:149], v[50:65]
	v_add_f32_e32 v224, v82, v224
	v_add_f32_e32 v225, v83, v225
	v_add_f32_e32 v226, v84, v226
	v_add_f32_e32 v227, v85, v227
	v_cvt_pk_f16_f32 v152, v110, v111
	v_cvt_pk_f16_f32 v153, v112, v113
	ds_read_b64_tr_b16 v[106:107], v206 offset:36864
	ds_read_b64_tr_b16 v[108:109], v206 offset:37888
	s_waitcnt lgkmcnt(13)
	v_mfma_f32_32x32x16_f16 v[66:81], v[178:181], v[138:141], v[66:81]
	v_add_f32_e32 v224, v86, v224
	v_add_f32_e32 v225, v87, v225
	v_add_f32_e32 v226, v88, v226
	v_add_f32_e32 v227, v89, v227
	v_cvt_pk_f16_f32 v142, v82, v83
	v_cvt_pk_f16_f32 v143, v84, v85
	ds_read_b64_tr_b16 v[102:103], v207 offset:36864
	ds_read_b64_tr_b16 v[104:105], v207 offset:37888
	s_waitcnt lgkmcnt(14)
	v_mfma_f32_32x32x16_f16 v[50:65], v[166:169], v[138:141], v[50:65]
	v_add_f32_e32 v224, v90, v224
	v_add_f32_e32 v225, v91, v225
	v_add_f32_e32 v226, v92, v226
	v_add_f32_e32 v227, v93, v227
	v_cvt_pk_f16_f32 v144, v86, v87
	v_cvt_pk_f16_f32 v145, v88, v89
	ds_read_b64_tr_b16 v[98:99], v206 offset:38912
	ds_read_b64_tr_b16 v[100:101], v206 offset:39936
	s_waitcnt lgkmcnt(14)
	v_mfma_f32_32x32x16_f16 v[66:81], v[170:173], v[134:137], v[66:81]
	v_add_f32_e32 v224, v94, v224
	v_add_f32_e32 v225, v95, v225
	v_add_f32_e32 v226, v96, v226
	v_add_f32_e32 v227, v97, v227
	v_cvt_pk_f16_f32 v130, v90, v91
	v_cvt_pk_f16_f32 v131, v92, v93
	ds_read_b64_tr_b16 v[86:87], v207 offset:38912
	ds_read_b64_tr_b16 v[88:89], v207 offset:39936
	v_mfma_f32_32x32x16_f16 v[50:65], v[162:165], v[134:137], v[50:65]
	v_add_f32_e32 v224, v224, v225
	v_add_f32_e32 v226, v226, v227
	v_add_f32_e32 v84, v224, v226
	v_cvt_pk_f16_f32 v132, v94, v95
	v_cvt_pk_f16_f32 v133, v96, v97
	s_add_u32 s54, s50, 0x2000
	s_addc_u32 s55, s51, 0
	s_add_i32 s26, s39, s36
	s_mov_b32 m0, s26
	s_nop 0
	global_load_lds_dwordx4 v221, s[54:55]
	v_max3_f32 v82, v66, v67, v68
	v_max3_f32 v83, v69, v70, v71
	v_max3_f32 v228, v72, v73, v74
	v_max3_f32 v229, v75, v76, v77
	v_max3_f32 v82, v82, v78, v79
	v_max3_f32 v83, v83, v80, v81
	v_max3_f32 v228, v228, v50, v51
	v_max3_f32 v229, v229, v52, v53
	v_max3_f32 v82, v82, v54, v55
	v_max3_f32 v83, v83, v56, v57
	v_max3_f32 v228, v228, v58, v59
	v_max3_f32 v229, v229, v60, v61
	v_max3_f32 v82, v82, v62, v63
	v_max3_f32 v83, v83, v64, v65
	v_max3_f32 v82, v82, v83, v228
	v_max_f32_e32 v82, v82, v229
	v_add_f32_e32 v183, v198, v84
	s_add_u32 s54, s52, 0x2000
	s_addc_u32 s55, s53, 0
	s_add_i32 s26, s43, s35
	s_mov_b32 m0, s26
	s_nop 0
	global_load_lds_dwordx4 v222, s[54:55]
	v_cmp_lt_f32_e32 vcc, s41, v82
	s_cmp_lg_u64 vcc, 0
	s_cselect_b64 s[26:27], -1, 0
	s_cbranch_vccnz .Lu0_12

.Lu1_1:
	ds_read_b64_tr_b16 v[178:179], v206 offset:40960
	ds_read_b64_tr_b16 v[180:181], v206 offset:41984
	s_waitcnt lgkmcnt(9)
	v_mfma_f32_32x32x16_f16 v[98:113], v[82:85], v[154:157], v[34:49]
	v_add_f32_e32 v224, v66, v70
	v_add_f32_e32 v225, v67, v71
	v_add_f32_e32 v226, v68, v72
	v_add_f32_e32 v227, v69, v73
	v_cvt_pk_f16_f32 v158, v66, v67
	v_cvt_pk_f16_f32 v159, v68, v69
	ds_read_b64_tr_b16 v[174:175], v207 offset:40960
	ds_read_b64_tr_b16 v[176:177], v207 offset:41984
	s_waitcnt lgkmcnt(10)
	v_mfma_f32_32x32x16_f16 v[82:97], v[170:173], v[154:157], v[34:49]
	v_add_f32_e32 v224, v74, v224
	v_add_f32_e32 v225, v75, v225
	v_add_f32_e32 v226, v76, v226
	v_add_f32_e32 v227, v77, v227
	v_cvt_pk_f16_f32 v160, v70, v71
	v_cvt_pk_f16_f32 v161, v72, v73
	ds_read_b64_tr_b16 v[170:171], v206 offset:43008
	ds_read_b64_tr_b16 v[172:173], v206 offset:44032
	s_waitcnt lgkmcnt(11)
	v_mfma_f32_32x32x16_f16 v[98:113], v[166:169], v[146:149], v[98:113]
	v_add_f32_e32 v224, v78, v224
	v_add_f32_e32 v225, v79, v225
	v_add_f32_e32 v226, v80, v226
	v_add_f32_e32 v227, v81, v227
	v_cvt_pk_f16_f32 v150, v74, v75
	v_cvt_pk_f16_f32 v151, v76, v77
	ds_read_b64_tr_b16 v[74:75], v207 offset:43008
	ds_read_b64_tr_b16 v[76:77], v207 offset:44032
	s_waitcnt lgkmcnt(12)
	v_mfma_f32_32x32x16_f16 v[82:97], v[162:165], v[146:149], v[82:97]
	v_add_f32_e32 v224, v50, v224
	v_add_f32_e32 v225, v51, v225
	v_add_f32_e32 v226, v52, v226
	v_add_f32_e32 v227, v53, v227
	v_cvt_pk_f16_f32 v152, v78, v79
	v_cvt_pk_f16_f32 v153, v80, v81
	ds_read_b64_tr_b16 v[70:71], v206 offset:45056
	ds_read_b64_tr_b16 v[72:73], v206 offset:46080
	s_waitcnt lgkmcnt(13)
	v_mfma_f32_32x32x16_f16 v[98:113], v[126:129], v[138:141], v[98:113]
	v_add_f32_e32 v224, v54, v224
	v_add_f32_e32 v225, v55, v225
	v_add_f32_e32 v226, v56, v226
	v_add_f32_e32 v227, v57, v227
	v_cvt_pk_f16_f32 v142, v50, v51
	v_cvt_pk_f16_f32 v143, v52, v53
	ds_read_b64_tr_b16 v[66:67], v207 offset:45056
	ds_read_b64_tr_b16 v[68:69], v207 offset:46080
	s_waitcnt lgkmcnt(14)
	v_mfma_f32_32x32x16_f16 v[82:97], v[122:125], v[138:141], v[82:97]
	v_add_f32_e32 v224, v58, v224
	v_add_f32_e32 v225, v59, v225
	v_add_f32_e32 v226, v60, v226
	v_add_f32_e32 v227, v61, v227
	v_cvt_pk_f16_f32 v144, v54, v55
	v_cvt_pk_f16_f32 v145, v56, v57
	ds_read_b64_tr_b16 v[54:55], v206 offset:47104
	ds_read_b64_tr_b16 v[56:57], v206 offset:48128
	s_waitcnt lgkmcnt(14)
	v_mfma_f32_32x32x16_f16 v[98:113], v[118:121], v[134:137], v[98:113]
	v_add_f32_e32 v224, v62, v224
	v_add_f32_e32 v225, v63, v225
	v_add_f32_e32 v226, v64, v226
	v_add_f32_e32 v227, v65, v227
	v_cvt_pk_f16_f32 v130, v58, v59
	v_cvt_pk_f16_f32 v131, v60, v61
	ds_read_b64_tr_b16 v[50:51], v207 offset:47104
	ds_read_b64_tr_b16 v[52:53], v207 offset:48128
	v_mfma_f32_32x32x16_f16 v[82:97], v[114:117], v[134:137], v[82:97]
	v_add_f32_e32 v224, v224, v225
	v_add_f32_e32 v226, v226, v227
	v_add_f32_e32 v60, v224, v226
	v_cvt_pk_f16_f32 v132, v62, v63
	v_cvt_pk_f16_f32 v133, v64, v65
	s_add_i32 s26, s42, s36
	s_mov_b32 m0, s26
	s_nop 0
	global_load_lds_dwordx4 v221, s[50:51]
	s_add_i32 s26, s39, s35
	s_mov_b32 m0, s26
	s_nop 0
	global_load_lds_dwordx4 v222, s[52:53]
	v_max3_f32 v58, v98, v99, v100
	v_max3_f32 v59, v101, v102, v103
	v_max3_f32 v228, v104, v105, v106
	v_max3_f32 v229, v107, v108, v109
	v_max3_f32 v58, v58, v110, v111
	v_max3_f32 v59, v59, v112, v113
	v_max3_f32 v228, v228, v82, v83
	v_max3_f32 v229, v229, v84, v85
	v_max3_f32 v58, v58, v86, v87
	v_max3_f32 v59, v59, v88, v89
	v_max3_f32 v228, v228, v90, v91
	v_max3_f32 v229, v229, v92, v93
	v_max3_f32 v58, v58, v94, v95
	v_max3_f32 v59, v59, v96, v97
	v_max3_f32 v58, v58, v59, v228
	v_max_f32_e32 v58, v58, v229
	v_add_f32_e32 v198, v183, v60
	v_cmp_lt_f32_e32 vcc, s41, v58
	s_cmp_lg_u64 vcc, 0
	s_cselect_b64 s[26:27], -1, 0
	s_cbranch_vccnz .Lu1_9

.Lu1_4:
	s_add_i32 s26, s39, 0x2000
	s_cmpk_lg_i32 s39, 0x4000
	s_cselect_b32 s43, s26, 0
	ds_read_b64_tr_b16 v[126:127], v206 offset:24576
	ds_read_b64_tr_b16 v[128:129], v206 offset:25600
	s_waitcnt lgkmcnt(9)
	v_mfma_f32_32x32x16_f16 v[66:81], v[58:61], v[154:157], v[34:49]
	v_add_f32_e32 v224, v98, v102
	v_add_f32_e32 v225, v99, v103
	v_add_f32_e32 v226, v100, v104
	v_add_f32_e32 v227, v101, v105
	v_cvt_pk_f16_f32 v158, v98, v99
	v_cvt_pk_f16_f32 v159, v100, v101
	ds_read_b64_tr_b16 v[122:123], v207 offset:24576
	ds_read_b64_tr_b16 v[124:125], v207 offset:25600
	s_waitcnt lgkmcnt(10)
	v_mfma_f32_32x32x16_f16 v[50:65], v[114:117], v[154:157], v[34:49]
	v_add_f32_e32 v224, v106, v224
	v_add_f32_e32 v225, v107, v225
	v_add_f32_e32 v226, v108, v226
	v_add_f32_e32 v227, v109, v227
	v_cvt_pk_f16_f32 v160, v102, v103
	v_cvt_pk_f16_f32 v161, v104, v105
	ds_read_b64_tr_b16 v[118:119], v206 offset:26624
	ds_read_b64_tr_b16 v[120:121], v206 offset:27648
	s_waitcnt lgkmcnt(11)
	v_mfma_f32_32x32x16_f16 v[66:81], v[182:185], v[146:149], v[66:81]
	v_add_f32_e32 v224, v110, v224
	v_add_f32_e32 v225, v111, v225
	v_add_f32_e32 v226, v112, v226
	v_add_f32_e32 v227, v113, v227
	v_cvt_pk_f16_f32 v150, v106, v107
	v_cvt_pk_f16_f32 v151, v108, v109
	ds_read_b64_tr_b16 v[114:115], v207 offset:26624
	ds_read_b64_tr_b16 v[116:117], v207 offset:27648
	s_waitcnt lgkmcnt(12)
	v_mfma_f32_32x32x16_f16 v[50:65], v[174:177], v[146:149], v[50:65]
	v_add_f32_e32 v224, v82, v224
	v_add_f32_e32 v225, v83, v225
	v_add_f32_e32 v226, v84, v226
	v_add_f32_e32 v227, v85, v227
	v_cvt_pk_f16_f32 v152, v110, v111
	v_cvt_pk_f16_f32 v153, v112, v113
	ds_read_b64_tr_b16 v[106:107], v206 offset:28672
	ds_read_b64_tr_b16 v[108:109], v206 offset:29696
	s_waitcnt lgkmcnt(13)
	v_mfma_f32_32x32x16_f16 v[66:81], v[178:181], v[138:141], v[66:81]
	v_add_f32_e32 v224, v86, v224
	v_add_f32_e32 v225, v87, v225
	v_add_f32_e32 v226, v88, v226
	v_add_f32_e32 v227, v89, v227
	v_cvt_pk_f16_f32 v142, v82, v83
	v_cvt_pk_f16_f32 v143, v84, v85
	ds_read_b64_tr_b16 v[102:103], v207 offset:28672
	ds_read_b64_tr_b16 v[104:105], v207 offset:29696
	s_waitcnt lgkmcnt(14)
	v_mfma_f32_32x32x16_f16 v[50:65], v[166:169], v[138:141], v[50:65]
	v_add_f32_e32 v224, v90, v224
	v_add_f32_e32 v225, v91, v225
	v_add_f32_e32 v226, v92, v226
	v_add_f32_e32 v227, v93, v227
	v_cvt_pk_f16_f32 v144, v86, v87
	v_cvt_pk_f16_f32 v145, v88, v89
	ds_read_b64_tr_b16 v[98:99], v206 offset:30720
	ds_read_b64_tr_b16 v[100:101], v206 offset:31744
	s_waitcnt lgkmcnt(14)
	v_mfma_f32_32x32x16_f16 v[66:81], v[170:173], v[134:137], v[66:81]
	v_add_f32_e32 v224, v94, v224
	v_add_f32_e32 v225, v95, v225
	v_add_f32_e32 v226, v96, v226
	v_add_f32_e32 v227, v97, v227
	v_cvt_pk_f16_f32 v130, v90, v91
	v_cvt_pk_f16_f32 v131, v92, v93
	ds_read_b64_tr_b16 v[86:87], v207 offset:30720
	ds_read_b64_tr_b16 v[88:89], v207 offset:31744
	v_mfma_f32_32x32x16_f16 v[50:65], v[162:165], v[134:137], v[50:65]
	v_add_f32_e32 v224, v224, v225
	v_add_f32_e32 v226, v226, v227
	v_add_f32_e32 v84, v224, v226
	v_cvt_pk_f16_f32 v132, v94, v95
	v_cvt_pk_f16_f32 v133, v96, v97
	s_add_u32 s54, s50, 0x2000
	s_addc_u32 s55, s51, 0
	s_add_i32 s26, s39, s36
	s_mov_b32 m0, s26
	s_nop 0
	global_load_lds_dwordx4 v221, s[54:55]
	v_max3_f32 v82, v66, v67, v68
	v_max3_f32 v83, v69, v70, v71
	v_max3_f32 v228, v72, v73, v74
	v_max3_f32 v229, v75, v76, v77
	v_max3_f32 v82, v82, v78, v79
	v_max3_f32 v83, v83, v80, v81
	v_max3_f32 v228, v228, v50, v51
	v_max3_f32 v229, v229, v52, v53
	v_max3_f32 v82, v82, v54, v55
	v_max3_f32 v83, v83, v56, v57
	v_max3_f32 v228, v228, v58, v59
	v_max3_f32 v229, v229, v60, v61
	v_max3_f32 v82, v82, v62, v63
	v_max3_f32 v83, v83, v64, v65
	v_max3_f32 v82, v82, v83, v228
	v_max_f32_e32 v82, v82, v229
	v_add_f32_e32 v183, v198, v84
	s_add_u32 s54, s52, 0x2000
	s_addc_u32 s55, s53, 0
	s_add_i32 s26, s43, s35
	s_mov_b32 m0, s26
	s_nop 0
	global_load_lds_dwordx4 v222, s[54:55]
	v_cmp_lt_f32_e32 vcc, s41, v82
	s_cmp_lg_u64 vcc, 0
	s_cselect_b64 s[26:27], -1, 0
	s_cbranch_vccnz .Lu1_12

.Lu2_1:
	ds_read_b64_tr_b16 v[178:179], v206 offset:32768
	ds_read_b64_tr_b16 v[180:181], v206 offset:33792
	s_waitcnt lgkmcnt(9)
	v_mfma_f32_32x32x16_f16 v[98:113], v[82:85], v[154:157], v[34:49]
	v_add_f32_e32 v224, v66, v70
	v_add_f32_e32 v225, v67, v71
	v_add_f32_e32 v226, v68, v72
	v_add_f32_e32 v227, v69, v73
	v_cvt_pk_f16_f32 v158, v66, v67
	v_cvt_pk_f16_f32 v159, v68, v69
	ds_read_b64_tr_b16 v[174:175], v207 offset:32768
	ds_read_b64_tr_b16 v[176:177], v207 offset:33792
	s_waitcnt lgkmcnt(10)
	v_mfma_f32_32x32x16_f16 v[82:97], v[170:173], v[154:157], v[34:49]
	v_add_f32_e32 v224, v74, v224
	v_add_f32_e32 v225, v75, v225
	v_add_f32_e32 v226, v76, v226
	v_add_f32_e32 v227, v77, v227
	v_cvt_pk_f16_f32 v160, v70, v71
	v_cvt_pk_f16_f32 v161, v72, v73
	ds_read_b64_tr_b16 v[170:171], v206 offset:34816
	ds_read_b64_tr_b16 v[172:173], v206 offset:35840
	s_waitcnt lgkmcnt(11)
	v_mfma_f32_32x32x16_f16 v[98:113], v[166:169], v[146:149], v[98:113]
	v_add_f32_e32 v224, v78, v224
	v_add_f32_e32 v225, v79, v225
	v_add_f32_e32 v226, v80, v226
	v_add_f32_e32 v227, v81, v227
	v_cvt_pk_f16_f32 v150, v74, v75
	v_cvt_pk_f16_f32 v151, v76, v77
	ds_read_b64_tr_b16 v[74:75], v207 offset:34816
	ds_read_b64_tr_b16 v[76:77], v207 offset:35840
	s_waitcnt lgkmcnt(12)
	v_mfma_f32_32x32x16_f16 v[82:97], v[162:165], v[146:149], v[82:97]
	v_add_f32_e32 v224, v50, v224
	v_add_f32_e32 v225, v51, v225
	v_add_f32_e32 v226, v52, v226
	v_add_f32_e32 v227, v53, v227
	v_cvt_pk_f16_f32 v152, v78, v79
	v_cvt_pk_f16_f32 v153, v80, v81
	ds_read_b64_tr_b16 v[70:71], v206 offset:36864
	ds_read_b64_tr_b16 v[72:73], v206 offset:37888
	s_waitcnt lgkmcnt(13)
	v_mfma_f32_32x32x16_f16 v[98:113], v[126:129], v[138:141], v[98:113]
	v_add_f32_e32 v224, v54, v224
	v_add_f32_e32 v225, v55, v225
	v_add_f32_e32 v226, v56, v226
	v_add_f32_e32 v227, v57, v227
	v_cvt_pk_f16_f32 v142, v50, v51
	v_cvt_pk_f16_f32 v143, v52, v53
	ds_read_b64_tr_b16 v[66:67], v207 offset:36864
	ds_read_b64_tr_b16 v[68:69], v207 offset:37888
	s_waitcnt lgkmcnt(14)
	v_mfma_f32_32x32x16_f16 v[82:97], v[122:125], v[138:141], v[82:97]
	v_add_f32_e32 v224, v58, v224
	v_add_f32_e32 v225, v59, v225
	v_add_f32_e32 v226, v60, v226
	v_add_f32_e32 v227, v61, v227
	v_cvt_pk_f16_f32 v144, v54, v55
	v_cvt_pk_f16_f32 v145, v56, v57
	ds_read_b64_tr_b16 v[54:55], v206 offset:38912
	ds_read_b64_tr_b16 v[56:57], v206 offset:39936
	s_waitcnt lgkmcnt(14)
	v_mfma_f32_32x32x16_f16 v[98:113], v[118:121], v[134:137], v[98:113]
	v_add_f32_e32 v224, v62, v224
	v_add_f32_e32 v225, v63, v225
	v_add_f32_e32 v226, v64, v226
	v_add_f32_e32 v227, v65, v227
	v_cvt_pk_f16_f32 v130, v58, v59
	v_cvt_pk_f16_f32 v131, v60, v61
	ds_read_b64_tr_b16 v[50:51], v207 offset:38912
	ds_read_b64_tr_b16 v[52:53], v207 offset:39936
	v_mfma_f32_32x32x16_f16 v[82:97], v[114:117], v[134:137], v[82:97]
	v_add_f32_e32 v224, v224, v225
	v_add_f32_e32 v226, v226, v227
	v_add_f32_e32 v60, v224, v226
	v_cvt_pk_f16_f32 v132, v62, v63
	v_cvt_pk_f16_f32 v133, v64, v65
	s_add_i32 s26, s42, s36
	s_mov_b32 m0, s26
	s_nop 0
	global_load_lds_dwordx4 v221, s[50:51]
	s_add_i32 s26, s39, s35
	s_mov_b32 m0, s26
	s_nop 0
	global_load_lds_dwordx4 v222, s[52:53]
	v_max3_f32 v58, v98, v99, v100
	v_max3_f32 v59, v101, v102, v103
	v_max3_f32 v228, v104, v105, v106
	v_max3_f32 v229, v107, v108, v109
	v_max3_f32 v58, v58, v110, v111
	v_max3_f32 v59, v59, v112, v113
	v_max3_f32 v228, v228, v82, v83
	v_max3_f32 v229, v229, v84, v85
	v_max3_f32 v58, v58, v86, v87
	v_max3_f32 v59, v59, v88, v89
	v_max3_f32 v228, v228, v90, v91
	v_max3_f32 v229, v229, v92, v93
	v_max3_f32 v58, v58, v94, v95
	v_max3_f32 v59, v59, v96, v97
	v_max3_f32 v58, v58, v59, v228
	v_max_f32_e32 v58, v58, v229
	v_add_f32_e32 v198, v183, v60
	v_cmp_lt_f32_e32 vcc, s41, v58
	s_cmp_lg_u64 vcc, 0
	s_cselect_b64 s[26:27], -1, 0
	s_cbranch_vccnz .Lu2_9

.Lu2_4:
	s_add_i32 s26, s39, 0x2000
	s_cmpk_lg_i32 s39, 0x4000
	s_cselect_b32 s43, s26, 0
	ds_read_b64_tr_b16 v[126:127], v206 offset:40960
	ds_read_b64_tr_b16 v[128:129], v206 offset:41984
	s_waitcnt lgkmcnt(9)
	v_mfma_f32_32x32x16_f16 v[66:81], v[58:61], v[154:157], v[34:49]
	v_add_f32_e32 v224, v98, v102
	v_add_f32_e32 v225, v99, v103
	v_add_f32_e32 v226, v100, v104
	v_add_f32_e32 v227, v101, v105
	v_cvt_pk_f16_f32 v158, v98, v99
	v_cvt_pk_f16_f32 v159, v100, v101
	ds_read_b64_tr_b16 v[122:123], v207 offset:40960
	ds_read_b64_tr_b16 v[124:125], v207 offset:41984
	s_waitcnt lgkmcnt(10)
	v_mfma_f32_32x32x16_f16 v[50:65], v[114:117], v[154:157], v[34:49]
	v_add_f32_e32 v224, v106, v224
	v_add_f32_e32 v225, v107, v225
	v_add_f32_e32 v226, v108, v226
	v_add_f32_e32 v227, v109, v227
	v_cvt_pk_f16_f32 v160, v102, v103
	v_cvt_pk_f16_f32 v161, v104, v105
	ds_read_b64_tr_b16 v[118:119], v206 offset:43008
	ds_read_b64_tr_b16 v[120:121], v206 offset:44032
	s_waitcnt lgkmcnt(11)
	v_mfma_f32_32x32x16_f16 v[66:81], v[182:185], v[146:149], v[66:81]
	v_add_f32_e32 v224, v110, v224
	v_add_f32_e32 v225, v111, v225
	v_add_f32_e32 v226, v112, v226
	v_add_f32_e32 v227, v113, v227
	v_cvt_pk_f16_f32 v150, v106, v107
	v_cvt_pk_f16_f32 v151, v108, v109
	ds_read_b64_tr_b16 v[114:115], v207 offset:43008
	ds_read_b64_tr_b16 v[116:117], v207 offset:44032
	s_waitcnt lgkmcnt(12)
	v_mfma_f32_32x32x16_f16 v[50:65], v[174:177], v[146:149], v[50:65]
	v_add_f32_e32 v224, v82, v224
	v_add_f32_e32 v225, v83, v225
	v_add_f32_e32 v226, v84, v226
	v_add_f32_e32 v227, v85, v227
	v_cvt_pk_f16_f32 v152, v110, v111
	v_cvt_pk_f16_f32 v153, v112, v113
	ds_read_b64_tr_b16 v[106:107], v206 offset:45056
	ds_read_b64_tr_b16 v[108:109], v206 offset:46080
	s_waitcnt lgkmcnt(13)
	v_mfma_f32_32x32x16_f16 v[66:81], v[178:181], v[138:141], v[66:81]
	v_add_f32_e32 v224, v86, v224
	v_add_f32_e32 v225, v87, v225
	v_add_f32_e32 v226, v88, v226
	v_add_f32_e32 v227, v89, v227
	v_cvt_pk_f16_f32 v142, v82, v83
	v_cvt_pk_f16_f32 v143, v84, v85
	ds_read_b64_tr_b16 v[102:103], v207 offset:45056
	ds_read_b64_tr_b16 v[104:105], v207 offset:46080
	s_waitcnt lgkmcnt(14)
	v_mfma_f32_32x32x16_f16 v[50:65], v[166:169], v[138:141], v[50:65]
	v_add_f32_e32 v224, v90, v224
	v_add_f32_e32 v225, v91, v225
	v_add_f32_e32 v226, v92, v226
	v_add_f32_e32 v227, v93, v227
	v_cvt_pk_f16_f32 v144, v86, v87
	v_cvt_pk_f16_f32 v145, v88, v89
	ds_read_b64_tr_b16 v[98:99], v206 offset:47104
	ds_read_b64_tr_b16 v[100:101], v206 offset:48128
	s_waitcnt lgkmcnt(14)
	v_mfma_f32_32x32x16_f16 v[66:81], v[170:173], v[134:137], v[66:81]
	v_add_f32_e32 v224, v94, v224
	v_add_f32_e32 v225, v95, v225
	v_add_f32_e32 v226, v96, v226
	v_add_f32_e32 v227, v97, v227
	v_cvt_pk_f16_f32 v130, v90, v91
	v_cvt_pk_f16_f32 v131, v92, v93
	ds_read_b64_tr_b16 v[86:87], v207 offset:47104
	ds_read_b64_tr_b16 v[88:89], v207 offset:48128
	v_mfma_f32_32x32x16_f16 v[50:65], v[162:165], v[134:137], v[50:65]
	v_add_f32_e32 v224, v224, v225
	v_add_f32_e32 v226, v226, v227
	v_add_f32_e32 v84, v224, v226
	v_cvt_pk_f16_f32 v132, v94, v95
	v_cvt_pk_f16_f32 v133, v96, v97
	s_add_u32 s54, s50, 0x2000
	s_addc_u32 s55, s51, 0
	s_add_i32 s26, s39, s36
	s_mov_b32 m0, s26
	s_nop 0
	global_load_lds_dwordx4 v221, s[54:55]
	v_max3_f32 v82, v66, v67, v68
	v_max3_f32 v83, v69, v70, v71
	v_max3_f32 v228, v72, v73, v74
	v_max3_f32 v229, v75, v76, v77
	v_max3_f32 v82, v82, v78, v79
	v_max3_f32 v83, v83, v80, v81
	v_max3_f32 v228, v228, v50, v51
	v_max3_f32 v229, v229, v52, v53
	v_max3_f32 v82, v82, v54, v55
	v_max3_f32 v83, v83, v56, v57
	v_max3_f32 v228, v228, v58, v59
	v_max3_f32 v229, v229, v60, v61
	v_max3_f32 v82, v82, v62, v63
	v_max3_f32 v83, v83, v64, v65
	v_max3_f32 v82, v82, v83, v228
	v_max_f32_e32 v82, v82, v229
	v_add_f32_e32 v183, v198, v84
	s_add_u32 s54, s52, 0x2000
	s_addc_u32 s55, s53, 0
	s_add_i32 s26, s43, s35
	s_mov_b32 m0, s26
	s_nop 0
	global_load_lds_dwordx4 v222, s[54:55]
	v_cmp_lt_f32_e32 vcc, s41, v82
	s_cmp_lg_u64 vcc, 0
	s_cselect_b64 s[26:27], -1, 0
	s_cbranch_vccnz .Lu2_12
